# baseline (speedup 1.0000x reference)
.Lp_main:
	v_and_b32_e32 v162, 63, v0
	s_getpc_b64 s[44:45]
	v_lshlrev_b32_e32 v162, 7, v162
	global_load_dword v162, v162, s[44:45]
	s_load_dwordx2 s[10:11], s[0:1], 0x0
	s_load_dwordx4 s[12:15], s[0:1], 0x10
	s_load_dwordx2 s[16:17], s[0:1], 0x20
	s_load_dwordx4 s[20:23], s[0:1], 0x28
	v_readfirstlane_b32 s3, v0
	v_and_b32_e32 v154, 63, v0
	v_lshrrev_b32_e32 v155, 5, v154
	v_lshlrev_b32_e32 v156, 4, v0
	v_lshlrev_b32_e32 v157, 4, v154
	v_lshlrev_b32_e32 v158, 8, v1
	v_lshl_add_u32 v158, v155, 5, v158
	v_lshlrev_b32_e32 v159, 4, v155
	v_lshrrev_b32_e32 v160, 3, v0
	v_lshlrev_b32_e32 v160, 12, v160
	v_and_b32_e32 v161, 7, v0
	v_lshl_add_u32 v160, v161, 4, v160
	s_lshr_b32 s41, s2, 3
	s_and_b32 s42, s2, 7
	s_lshl_b32 s24, s42, 2
	s_bfe_u32 s25, s2, 0x20003
	s_add_u32 s24, s24, s25
	s_lshr_b32 s25, s2, 5
	s_lshr_b32 s26, s3, 6
	s_lshl_b32 s27, s25, 2
	s_add_u32 s27, s27, s26
	s_mov_b32 s4, 0x4038aa3b
	s_mov_b32 s5, s4
	s_lshl_b32 s40, s26, 6
	s_waitcnt lgkmcnt(0)
	s_lshl_b32 s28, s24, 15
	s_add_u32 s28, s28, 0x1000
	s_add_u32 s10, s10, s28
	s_addc_u32 s11, s11, 0
	s_lshl_b32 s34, s41, 17
	s_lshl_b32 s35, s42, 9
	s_add_u32 s34, s34, s35
	s_add_u32 s34, s14, s34
	s_addc_u32 s35, s15, 0
	s_lshl_b32 s28, s27, 13
	s_add_u32 s28, s8, s28
	s_addc_u32 s29, s9, 0
	s_lshl_b32 s30, s27, 7
	s_add_u32 s30, s12, s30
	s_addc_u32 s31, s13, 0
	global_load_dwordx4 v[2:5], v156, s[10:11] offset:-4096
	global_load_dwordx4 v[6:9], v156, s[10:11] offset:0
	s_add_u32 s10, s10, 0x2000
	s_addc_u32 s11, s11, 0
	global_load_dwordx4 v[10:13], v156, s[10:11] offset:-4096
	global_load_dwordx4 v[14:17], v156, s[10:11] offset:0
	s_add_u32 s10, s10, 0x2000
	s_addc_u32 s11, s11, 0
	global_load_dwordx4 v[18:21], v156, s[10:11] offset:-4096
	global_load_dwordx4 v[22:25], v156, s[10:11] offset:0
	s_add_u32 s10, s10, 0x2000
	s_addc_u32 s11, s11, 0
	global_load_dwordx4 v[26:29], v156, s[10:11] offset:-4096
	global_load_dwordx4 v[30:33], v156, s[10:11] offset:0
	global_load_dwordx4 v[130:133], v160, s[34:35] offset:0
	global_load_dwordx4 v[134:137], v160, s[34:35] offset:128
	global_load_dwordx4 v[138:141], v160, s[34:35] offset:256
	global_load_dwordx4 v[142:145], v160, s[34:35] offset:384
	global_load_dwordx4 v[34:37], v158, s[28:29] offset:0
	global_load_dwordx4 v[38:41], v158, s[28:29] offset:16
	global_load_dwordx4 v[42:45], v158, s[28:29] offset:64
	global_load_dwordx4 v[46:49], v158, s[28:29] offset:80
	global_load_dwordx4 v[50:53], v158, s[28:29] offset:128
	global_load_dwordx4 v[54:57], v158, s[28:29] offset:144
	global_load_dwordx4 v[58:61], v158, s[28:29] offset:192
	global_load_dwordx4 v[62:65], v158, s[28:29] offset:208
	global_load_dwordx4 v[66:69], v159, s[30:31] offset:0
	global_load_dwordx4 v[70:73], v159, s[30:31] offset:32
	global_load_dwordx4 v[74:77], v159, s[30:31] offset:64
	global_load_dwordx4 v[78:81], v159, s[30:31] offset:96
	v_bfe_u32 v163, v0, 1, 3
	v_mul_u32_u24_e32 v163, 0x210, v163
	v_lshrrev_b32_e32 v164, 4, v0
	v_lshl_add_u32 v163, v164, 4, v163
	v_and_b32_e32 v164, 1, v0
	v_lshl_add_u32 v163, v164, 3, v163
	v_lshrrev_b32_e32 v164, 3, v0
	v_mul_u32_u24_e32 v164, 0x110, v164
	v_lshl_add_u32 v164, v161, 3, v164
	v_add_u32_e32 v164, 0x4200, v164
	v_mul_u32_u24_e32 v165, 0x210, v155
	v_lshl_add_u32 v165, v1, 4, v165
	v_mul_u32_u24_e32 v166, 0x110, v1
	v_lshl_add_u32 v166, v155, 4, v166
	v_add_u32_e32 v166, s40, v166
	v_add_u32_e32 v166, 0x4200, v166
	v_mul_u32_u24_e32 v167, 0x880, v155
	v_lshl_add_u32 v167, v1, 1, v167
	v_add_u32_e32 v167, s40, v167
	v_add_u32_e32 v167, 0x4200, v167
	s_lshl_b32 s32, s24, 18
	s_lshl_b32 s33, s27, 11
	s_add_u32 s32, s32, s33
	s_add_u32 s32, s16, s32
	s_addc_u32 s33, s17, 0
	s_lshl_b32 s36, s41, 16
	s_lshl_b32 s37, s42, 13
	s_add_u32 s36, s36, s37
	s_lshl_b32 s37, s26, 11
	s_add_u32 s36, s36, s37
	s_add_u32 s36, s20, s36
	s_addc_u32 s37, s21, 0
	s_lshl_b32 s38, s42, 18
	s_lshl_b32 s39, s26, 16
	s_add_u32 s38, s38, s39
	s_lshl_b32 s39, s41, 11
	s_add_u32 s38, s38, s39
	s_add_u32 s38, s22, s38
	s_addc_u32 s39, s23, 0
	s_waitcnt vmcnt(23)
	v_cvt_pk_f16_f32 v2, v2, v3
	v_cvt_pk_f16_f32 v3, v4, v5
	ds_write_b64 v163, v[2:3] offset:0
	s_waitcnt vmcnt(22)
	v_cvt_pk_f16_f32 v6, v6, v7
	v_cvt_pk_f16_f32 v7, v8, v9
	ds_write_b64 v163, v[6:7] offset:256
	s_waitcnt vmcnt(21)
	v_cvt_pk_f16_f32 v10, v10, v11
	v_cvt_pk_f16_f32 v11, v12, v13
	ds_write_b64 v163, v[10:11] offset:4224
	s_waitcnt vmcnt(20)
	v_cvt_pk_f16_f32 v14, v14, v15
	v_cvt_pk_f16_f32 v15, v16, v17
	ds_write_b64 v163, v[14:15] offset:4480
	s_waitcnt vmcnt(19)
	v_cvt_pk_f16_f32 v18, v18, v19
	v_cvt_pk_f16_f32 v19, v20, v21
	ds_write_b64 v163, v[18:19] offset:8448
	s_waitcnt vmcnt(18)
	v_cvt_pk_f16_f32 v22, v22, v23
	v_cvt_pk_f16_f32 v23, v24, v25
	ds_write_b64 v163, v[22:23] offset:8704
	s_waitcnt vmcnt(17)
	v_cvt_pk_f16_f32 v26, v26, v27
	v_cvt_pk_f16_f32 v27, v28, v29
	ds_write_b64 v163, v[26:27] offset:12672
	s_waitcnt vmcnt(16)
	v_cvt_pk_f16_f32 v30, v30, v31
	v_cvt_pk_f16_f32 v31, v32, v33
	ds_write_b64 v163, v[30:31] offset:12928
	s_waitcnt vmcnt(15)
	v_cvt_pk_f16_f32 v130, v130, v131
	v_cvt_pk_f16_f32 v131, v132, v133
	ds_write_b64 v164, v[130:131] offset:0
	s_waitcnt vmcnt(14)
	v_cvt_pk_f16_f32 v134, v134, v135
	v_cvt_pk_f16_f32 v135, v136, v137
	ds_write_b64 v164, v[134:135] offset:64
	s_waitcnt vmcnt(13)
	v_cvt_pk_f16_f32 v138, v138, v139
	v_cvt_pk_f16_f32 v139, v140, v141
	ds_write_b64 v164, v[138:139] offset:128
	s_waitcnt vmcnt(12)
	v_cvt_pk_f16_f32 v142, v142, v143
	v_cvt_pk_f16_f32 v143, v144, v145
	ds_write_b64 v164, v[142:143] offset:192
	s_waitcnt lgkmcnt(0)
	s_barrier
	ds_read_b128 v[130:133], v166
	ds_read_b128 v[134:137], v166 offset:32
	ds_read_u16 v138, v167 offset:0
	ds_read_u16 v139, v167 offset:272
	ds_read_u16 v140, v167 offset:544
	ds_read_u16 v141, v167 offset:816
	ds_read_u16 v142, v167 offset:1088
	ds_read_u16 v143, v167 offset:1360
	ds_read_u16 v144, v167 offset:1632
	ds_read_u16 v145, v167 offset:1904
	s_waitcnt vmcnt(4)
	v_cvt_pk_f16_f32 v82, v34, v35
	v_cvt_pk_f16_f32 v83, v36, v37
	v_cvt_pk_f16_f32 v84, v38, v39
	v_cvt_pk_f16_f32 v85, v40, v41
	v_cvt_pk_f16_f32 v86, v42, v43
	v_cvt_pk_f16_f32 v87, v44, v45
	v_cvt_pk_f16_f32 v88, v46, v47
	v_cvt_pk_f16_f32 v89, v48, v49
	v_cvt_pk_f16_f32 v90, v50, v51
	v_cvt_pk_f16_f32 v91, v52, v53
	v_cvt_pk_f16_f32 v92, v54, v55
	v_cvt_pk_f16_f32 v93, v56, v57
	v_cvt_pk_f16_f32 v94, v58, v59
	v_cvt_pk_f16_f32 v95, v60, v61
	v_cvt_pk_f16_f32 v96, v62, v63
	v_cvt_pk_f16_f32 v97, v64, v65
	s_waitcnt vmcnt(0)
	v_pk_mul_f32 v[66:67], v[66:67], s[4:5] op_sel_hi:[1,0]
	v_pk_mul_f32 v[68:69], v[68:69], s[4:5] op_sel_hi:[1,0]
	v_pk_mul_f32 v[70:71], v[70:71], s[4:5] op_sel_hi:[1,0]
	v_pk_mul_f32 v[72:73], v[72:73], s[4:5] op_sel_hi:[1,0]
	v_pk_mul_f32 v[74:75], v[74:75], s[4:5] op_sel_hi:[1,0]
	v_pk_mul_f32 v[76:77], v[76:77], s[4:5] op_sel_hi:[1,0]
	v_pk_mul_f32 v[78:79], v[78:79], s[4:5] op_sel_hi:[1,0]
	v_pk_mul_f32 v[80:81], v[80:81], s[4:5] op_sel_hi:[1,0]
	s_waitcnt lgkmcnt(8)
	global_store_dwordx4 v157, v[130:133], s[36:37] sc1
	global_store_dwordx4 v157, v[134:137], s[36:37] offset:1024 sc1
	s_waitcnt lgkmcnt(0)
	v_lshl_or_b32 v138, v139, 16, v138
	v_lshl_or_b32 v139, v141, 16, v140
	v_lshl_or_b32 v140, v143, 16, v142
	v_lshl_or_b32 v141, v145, 16, v144
	global_store_dwordx4 v157, v[138:141], s[38:39] sc1
	ds_read_u16 v142, v167 offset:4352
	ds_read_u16 v143, v167 offset:4624
	ds_read_u16 v144, v167 offset:4896
	ds_read_u16 v145, v167 offset:5168
	ds_read_u16 v146, v167 offset:5440
	ds_read_u16 v147, v167 offset:5712
	ds_read_u16 v148, v167 offset:5984
	ds_read_u16 v149, v167 offset:6256
	ds_read_b128 v[2:5], v165 offset:0
	ds_read_b128 v[6:9], v165 offset:1056
	ds_read_b128 v[10:13], v165 offset:2112
	ds_read_b128 v[14:17], v165 offset:3168
	s_waitcnt lgkmcnt(4)
	v_lshl_or_b32 v142, v143, 16, v142
	v_lshl_or_b32 v143, v145, 16, v144
	v_lshl_or_b32 v144, v147, 16, v146
	v_lshl_or_b32 v145, v149, 16, v148
	global_store_dwordx4 v157, v[142:145], s[38:39] offset:1024 sc1
	ds_read_b128 v[18:21], v165 offset:4224
	ds_read_b128 v[22:25], v165 offset:5280
	ds_read_b128 v[26:29], v165 offset:6336
	ds_read_b128 v[30:33], v165 offset:7392
	ds_read_b128 v[34:37], v165 offset:8448
	ds_read_b128 v[38:41], v165 offset:9504
	ds_read_b128 v[42:45], v165 offset:10560
	ds_read_b128 v[46:49], v165 offset:11616
	s_waitcnt lgkmcnt(8)
	v_mfma_f32_32x32x16_f16 v[98:113], v[82:85], v[2:5], 0
	v_mfma_f32_32x32x16_f16 v[98:113], v[86:89], v[6:9], v[98:113]
	v_mfma_f32_32x32x16_f16 v[98:113], v[90:93], v[10:13], v[98:113]
	v_mfma_f32_32x32x16_f16 v[98:113], v[94:97], v[14:17], v[98:113]
	ds_read_b128 v[50:53], v165 offset:12672
	ds_read_b128 v[54:57], v165 offset:13728
	ds_read_b128 v[58:61], v165 offset:14784
	ds_read_b128 v[62:65], v165 offset:15840
	s_waitcnt lgkmcnt(8)
	v_mfma_f32_32x32x16_f16 v[114:129], v[82:85], v[18:21], 0
	v_mfma_f32_32x32x16_f16 v[114:129], v[86:89], v[22:25], v[114:129]
	v_mfma_f32_32x32x16_f16 v[114:129], v[90:93], v[26:29], v[114:129]
	v_mfma_f32_32x32x16_f16 v[114:129], v[94:97], v[30:33], v[114:129]
	s_nop 7
	v_pk_fma_f32 v[130:131], v[98:99], s[4:5], v[66:67] op_sel_hi:[1,0,1]
	v_pk_fma_f32 v[132:133], v[100:101], s[4:5], v[68:69] op_sel_hi:[1,0,1]
	v_pk_fma_f32 v[134:135], v[102:103], s[4:5], v[70:71] op_sel_hi:[1,0,1]
	v_pk_fma_f32 v[136:137], v[104:105], s[4:5], v[72:73] op_sel_hi:[1,0,1]
	v_pk_fma_f32 v[138:139], v[106:107], s[4:5], v[74:75] op_sel_hi:[1,0,1]
	v_pk_fma_f32 v[140:141], v[108:109], s[4:5], v[76:77] op_sel_hi:[1,0,1]
	v_pk_fma_f32 v[142:143], v[110:111], s[4:5], v[78:79] op_sel_hi:[1,0,1]
	v_pk_fma_f32 v[144:145], v[112:113], s[4:5], v[80:81] op_sel_hi:[1,0,1]
	v_exp_f32_e32 v130, v130
	v_exp_f32_e32 v131, v131
	v_exp_f32_e32 v132, v132
	v_exp_f32_e32 v133, v133
	v_exp_f32_e32 v134, v134
	v_exp_f32_e32 v135, v135
	v_exp_f32_e32 v136, v136
	v_exp_f32_e32 v137, v137
	v_exp_f32_e32 v138, v138
	v_exp_f32_e32 v139, v139
	v_exp_f32_e32 v140, v140
	v_exp_f32_e32 v141, v141
	v_exp_f32_e32 v142, v142
	v_exp_f32_e32 v143, v143
	v_exp_f32_e32 v144, v144
	v_exp_f32_e32 v145, v145
	v_pk_add_f32 v[130:131], v[130:131], 1.0 op_sel_hi:[1,0]
	v_pk_add_f32 v[132:133], v[132:133], 1.0 op_sel_hi:[1,0]
	v_pk_add_f32 v[134:135], v[134:135], 1.0 op_sel_hi:[1,0]
	v_pk_add_f32 v[136:137], v[136:137], 1.0 op_sel_hi:[1,0]
	v_pk_add_f32 v[138:139], v[138:139], 1.0 op_sel_hi:[1,0]
	v_pk_add_f32 v[140:141], v[140:141], 1.0 op_sel_hi:[1,0]
	v_pk_add_f32 v[142:143], v[142:143], 1.0 op_sel_hi:[1,0]
	v_pk_add_f32 v[144:145], v[144:145], 1.0 op_sel_hi:[1,0]
	v_rcp_f32_e32 v130, v130
	v_rcp_f32_e32 v131, v131
	v_rcp_f32_e32 v132, v132
	v_rcp_f32_e32 v133, v133
	v_rcp_f32_e32 v134, v134
	v_rcp_f32_e32 v135, v135
	v_rcp_f32_e32 v136, v136
	v_rcp_f32_e32 v137, v137
	v_rcp_f32_e32 v138, v138
	v_rcp_f32_e32 v139, v139
	v_rcp_f32_e32 v140, v140
	v_rcp_f32_e32 v141, v141
	v_rcp_f32_e32 v142, v142
	v_rcp_f32_e32 v143, v143
	v_rcp_f32_e32 v144, v144
	v_rcp_f32_e32 v145, v145
	v_pk_fma_f32 v[130:131], v[130:131], 2.0, 1.0 op_sel_hi:[1,0,0] neg_lo:[1,0,0] neg_hi:[1,0,0]
	v_pk_fma_f32 v[132:133], v[132:133], 2.0, 1.0 op_sel_hi:[1,0,0] neg_lo:[1,0,0] neg_hi:[1,0,0]
	v_pk_fma_f32 v[134:135], v[134:135], 2.0, 1.0 op_sel_hi:[1,0,0] neg_lo:[1,0,0] neg_hi:[1,0,0]
	v_pk_fma_f32 v[136:137], v[136:137], 2.0, 1.0 op_sel_hi:[1,0,0] neg_lo:[1,0,0] neg_hi:[1,0,0]
	v_pk_fma_f32 v[138:139], v[138:139], 2.0, 1.0 op_sel_hi:[1,0,0] neg_lo:[1,0,0] neg_hi:[1,0,0]
	v_pk_fma_f32 v[140:141], v[140:141], 2.0, 1.0 op_sel_hi:[1,0,0] neg_lo:[1,0,0] neg_hi:[1,0,0]
	v_pk_fma_f32 v[142:143], v[142:143], 2.0, 1.0 op_sel_hi:[1,0,0] neg_lo:[1,0,0] neg_hi:[1,0,0]
	v_pk_fma_f32 v[144:145], v[144:145], 2.0, 1.0 op_sel_hi:[1,0,0] neg_lo:[1,0,0] neg_hi:[1,0,0]
	v_cvt_pk_f16_f32 v146, v130, v131
	v_cvt_pk_f16_f32 v147, v132, v133
	v_cvt_pk_f16_f32 v148, v134, v135
	v_cvt_pk_f16_f32 v149, v136, v137
	v_cvt_pk_f16_f32 v150, v138, v139
	v_cvt_pk_f16_f32 v151, v140, v141
	v_cvt_pk_f16_f32 v152, v142, v143
	v_cvt_pk_f16_f32 v153, v144, v145
	s_nop 1
	v_permlane32_swap_b32_e32 v146, v148
	v_permlane32_swap_b32_e32 v147, v149
	v_permlane32_swap_b32_e32 v150, v152
	v_permlane32_swap_b32_e32 v151, v153
	global_store_dwordx4 v157, v[146:149], s[32:33] sc1
	global_store_dwordx4 v157, v[150:153], s[32:33] offset:1024 sc1
	s_add_u32 s32, s32, 0x10000
	s_addc_u32 s33, s33, 0
	s_waitcnt lgkmcnt(4)
	v_mfma_f32_32x32x16_f16 v[98:113], v[82:85], v[34:37], 0
	v_mfma_f32_32x32x16_f16 v[98:113], v[86:89], v[38:41], v[98:113]
	v_mfma_f32_32x32x16_f16 v[98:113], v[90:93], v[42:45], v[98:113]
	v_mfma_f32_32x32x16_f16 v[98:113], v[94:97], v[46:49], v[98:113]
	v_pk_fma_f32 v[130:131], v[114:115], s[4:5], v[66:67] op_sel_hi:[1,0,1]
	v_pk_fma_f32 v[132:133], v[116:117], s[4:5], v[68:69] op_sel_hi:[1,0,1]
	v_pk_fma_f32 v[134:135], v[118:119], s[4:5], v[70:71] op_sel_hi:[1,0,1]
	v_pk_fma_f32 v[136:137], v[120:121], s[4:5], v[72:73] op_sel_hi:[1,0,1]
	v_pk_fma_f32 v[138:139], v[122:123], s[4:5], v[74:75] op_sel_hi:[1,0,1]
	v_pk_fma_f32 v[140:141], v[124:125], s[4:5], v[76:77] op_sel_hi:[1,0,1]
	v_pk_fma_f32 v[142:143], v[126:127], s[4:5], v[78:79] op_sel_hi:[1,0,1]
	v_pk_fma_f32 v[144:145], v[128:129], s[4:5], v[80:81] op_sel_hi:[1,0,1]
	v_exp_f32_e32 v130, v130
	v_exp_f32_e32 v131, v131
	v_exp_f32_e32 v132, v132
	v_exp_f32_e32 v133, v133
	v_exp_f32_e32 v134, v134
	v_exp_f32_e32 v135, v135
	v_exp_f32_e32 v136, v136
	v_exp_f32_e32 v137, v137
	v_exp_f32_e32 v138, v138
	v_exp_f32_e32 v139, v139
	v_exp_f32_e32 v140, v140
	v_exp_f32_e32 v141, v141
	v_exp_f32_e32 v142, v142
	v_exp_f32_e32 v143, v143
	v_exp_f32_e32 v144, v144
	v_exp_f32_e32 v145, v145
	v_pk_add_f32 v[130:131], v[130:131], 1.0 op_sel_hi:[1,0]
	v_pk_add_f32 v[132:133], v[132:133], 1.0 op_sel_hi:[1,0]
	v_pk_add_f32 v[134:135], v[134:135], 1.0 op_sel_hi:[1,0]
	v_pk_add_f32 v[136:137], v[136:137], 1.0 op_sel_hi:[1,0]
	v_pk_add_f32 v[138:139], v[138:139], 1.0 op_sel_hi:[1,0]
	v_pk_add_f32 v[140:141], v[140:141], 1.0 op_sel_hi:[1,0]
	v_pk_add_f32 v[142:143], v[142:143], 1.0 op_sel_hi:[1,0]
	v_pk_add_f32 v[144:145], v[144:145], 1.0 op_sel_hi:[1,0]
	v_rcp_f32_e32 v130, v130
	v_rcp_f32_e32 v131, v131
	v_rcp_f32_e32 v132, v132
	v_rcp_f32_e32 v133, v133
	v_rcp_f32_e32 v134, v134
	v_rcp_f32_e32 v135, v135
	v_rcp_f32_e32 v136, v136
	v_rcp_f32_e32 v137, v137
	v_rcp_f32_e32 v138, v138
	v_rcp_f32_e32 v139, v139
	v_rcp_f32_e32 v140, v140
	v_rcp_f32_e32 v141, v141
	v_rcp_f32_e32 v142, v142
	v_rcp_f32_e32 v143, v143
	v_rcp_f32_e32 v144, v144
	v_rcp_f32_e32 v145, v145
	v_pk_fma_f32 v[130:131], v[130:131], 2.0, 1.0 op_sel_hi:[1,0,0] neg_lo:[1,0,0] neg_hi:[1,0,0]
	v_pk_fma_f32 v[132:133], v[132:133], 2.0, 1.0 op_sel_hi:[1,0,0] neg_lo:[1,0,0] neg_hi:[1,0,0]
	v_pk_fma_f32 v[134:135], v[134:135], 2.0, 1.0 op_sel_hi:[1,0,0] neg_lo:[1,0,0] neg_hi:[1,0,0]
	v_pk_fma_f32 v[136:137], v[136:137], 2.0, 1.0 op_sel_hi:[1,0,0] neg_lo:[1,0,0] neg_hi:[1,0,0]
	v_pk_fma_f32 v[138:139], v[138:139], 2.0, 1.0 op_sel_hi:[1,0,0] neg_lo:[1,0,0] neg_hi:[1,0,0]
	v_pk_fma_f32 v[140:141], v[140:141], 2.0, 1.0 op_sel_hi:[1,0,0] neg_lo:[1,0,0] neg_hi:[1,0,0]
	v_pk_fma_f32 v[142:143], v[142:143], 2.0, 1.0 op_sel_hi:[1,0,0] neg_lo:[1,0,0] neg_hi:[1,0,0]
	v_pk_fma_f32 v[144:145], v[144:145], 2.0, 1.0 op_sel_hi:[1,0,0] neg_lo:[1,0,0] neg_hi:[1,0,0]
	v_cvt_pk_f16_f32 v146, v130, v131
	v_cvt_pk_f16_f32 v147, v132, v133
	v_cvt_pk_f16_f32 v148, v134, v135
	v_cvt_pk_f16_f32 v149, v136, v137
	v_cvt_pk_f16_f32 v150, v138, v139
	v_cvt_pk_f16_f32 v151, v140, v141
	v_cvt_pk_f16_f32 v152, v142, v143
	v_cvt_pk_f16_f32 v153, v144, v145
	s_nop 1
	v_permlane32_swap_b32_e32 v146, v148
	v_permlane32_swap_b32_e32 v147, v149
	v_permlane32_swap_b32_e32 v150, v152
	v_permlane32_swap_b32_e32 v151, v153
	global_store_dwordx4 v157, v[146:149], s[32:33] sc1
	global_store_dwordx4 v157, v[150:153], s[32:33] offset:1024 sc1
	s_add_u32 s32, s32, 0x10000
	s_addc_u32 s33, s33, 0
	s_waitcnt lgkmcnt(0)
	v_mfma_f32_32x32x16_f16 v[114:129], v[82:85], v[50:53], 0
	v_mfma_f32_32x32x16_f16 v[114:129], v[86:89], v[54:57], v[114:129]
	v_mfma_f32_32x32x16_f16 v[114:129], v[90:93], v[58:61], v[114:129]
	v_mfma_f32_32x32x16_f16 v[114:129], v[94:97], v[62:65], v[114:129]
	v_pk_fma_f32 v[130:131], v[98:99], s[4:5], v[66:67] op_sel_hi:[1,0,1]
	v_pk_fma_f32 v[132:133], v[100:101], s[4:5], v[68:69] op_sel_hi:[1,0,1]
	v_pk_fma_f32 v[134:135], v[102:103], s[4:5], v[70:71] op_sel_hi:[1,0,1]
	v_pk_fma_f32 v[136:137], v[104:105], s[4:5], v[72:73] op_sel_hi:[1,0,1]
	v_pk_fma_f32 v[138:139], v[106:107], s[4:5], v[74:75] op_sel_hi:[1,0,1]
	v_pk_fma_f32 v[140:141], v[108:109], s[4:5], v[76:77] op_sel_hi:[1,0,1]
	v_pk_fma_f32 v[142:143], v[110:111], s[4:5], v[78:79] op_sel_hi:[1,0,1]
	v_pk_fma_f32 v[144:145], v[112:113], s[4:5], v[80:81] op_sel_hi:[1,0,1]
	v_exp_f32_e32 v130, v130
	v_exp_f32_e32 v131, v131
	v_exp_f32_e32 v132, v132
	v_exp_f32_e32 v133, v133
	v_exp_f32_e32 v134, v134
	v_exp_f32_e32 v135, v135
	v_exp_f32_e32 v136, v136
	v_exp_f32_e32 v137, v137
	v_exp_f32_e32 v138, v138
	v_exp_f32_e32 v139, v139
	v_exp_f32_e32 v140, v140
	v_exp_f32_e32 v141, v141
	v_exp_f32_e32 v142, v142
	v_exp_f32_e32 v143, v143
	v_exp_f32_e32 v144, v144
	v_exp_f32_e32 v145, v145
	v_pk_add_f32 v[130:131], v[130:131], 1.0 op_sel_hi:[1,0]
	v_pk_add_f32 v[132:133], v[132:133], 1.0 op_sel_hi:[1,0]
	v_pk_add_f32 v[134:135], v[134:135], 1.0 op_sel_hi:[1,0]
	v_pk_add_f32 v[136:137], v[136:137], 1.0 op_sel_hi:[1,0]
	v_pk_add_f32 v[138:139], v[138:139], 1.0 op_sel_hi:[1,0]
	v_pk_add_f32 v[140:141], v[140:141], 1.0 op_sel_hi:[1,0]
	v_pk_add_f32 v[142:143], v[142:143], 1.0 op_sel_hi:[1,0]
	v_pk_add_f32 v[144:145], v[144:145], 1.0 op_sel_hi:[1,0]
	v_rcp_f32_e32 v130, v130
	v_rcp_f32_e32 v131, v131
	v_rcp_f32_e32 v132, v132
	v_rcp_f32_e32 v133, v133
	v_rcp_f32_e32 v134, v134
	v_rcp_f32_e32 v135, v135
	v_rcp_f32_e32 v136, v136
	v_rcp_f32_e32 v137, v137
	v_rcp_f32_e32 v138, v138
	v_rcp_f32_e32 v139, v139
	v_rcp_f32_e32 v140, v140
	v_rcp_f32_e32 v141, v141
	v_rcp_f32_e32 v142, v142
	v_rcp_f32_e32 v143, v143
	v_rcp_f32_e32 v144, v144
	v_rcp_f32_e32 v145, v145
	v_pk_fma_f32 v[130:131], v[130:131], 2.0, 1.0 op_sel_hi:[1,0,0] neg_lo:[1,0,0] neg_hi:[1,0,0]
	v_pk_fma_f32 v[132:133], v[132:133], 2.0, 1.0 op_sel_hi:[1,0,0] neg_lo:[1,0,0] neg_hi:[1,0,0]
	v_pk_fma_f32 v[134:135], v[134:135], 2.0, 1.0 op_sel_hi:[1,0,0] neg_lo:[1,0,0] neg_hi:[1,0,0]
	v_pk_fma_f32 v[136:137], v[136:137], 2.0, 1.0 op_sel_hi:[1,0,0] neg_lo:[1,0,0] neg_hi:[1,0,0]
	v_pk_fma_f32 v[138:139], v[138:139], 2.0, 1.0 op_sel_hi:[1,0,0] neg_lo:[1,0,0] neg_hi:[1,0,0]
	v_pk_fma_f32 v[140:141], v[140:141], 2.0, 1.0 op_sel_hi:[1,0,0] neg_lo:[1,0,0] neg_hi:[1,0,0]
	v_pk_fma_f32 v[142:143], v[142:143], 2.0, 1.0 op_sel_hi:[1,0,0] neg_lo:[1,0,0] neg_hi:[1,0,0]
	v_pk_fma_f32 v[144:145], v[144:145], 2.0, 1.0 op_sel_hi:[1,0,0] neg_lo:[1,0,0] neg_hi:[1,0,0]
	v_cvt_pk_f16_f32 v146, v130, v131
	v_cvt_pk_f16_f32 v147, v132, v133
	v_cvt_pk_f16_f32 v148, v134, v135
	v_cvt_pk_f16_f32 v149, v136, v137
	v_cvt_pk_f16_f32 v150, v138, v139
	v_cvt_pk_f16_f32 v151, v140, v141
	v_cvt_pk_f16_f32 v152, v142, v143
	v_cvt_pk_f16_f32 v153, v144, v145
	s_nop 1
	v_permlane32_swap_b32_e32 v146, v148
	v_permlane32_swap_b32_e32 v147, v149
	v_permlane32_swap_b32_e32 v150, v152
	v_permlane32_swap_b32_e32 v151, v153
	global_store_dwordx4 v157, v[146:149], s[32:33] sc1
	global_store_dwordx4 v157, v[150:153], s[32:33] offset:1024 sc1
	s_add_u32 s32, s32, 0x10000
	s_addc_u32 s33, s33, 0
	s_nop 7
	v_pk_fma_f32 v[130:131], v[114:115], s[4:5], v[66:67] op_sel_hi:[1,0,1]
	v_pk_fma_f32 v[132:133], v[116:117], s[4:5], v[68:69] op_sel_hi:[1,0,1]
	v_pk_fma_f32 v[134:135], v[118:119], s[4:5], v[70:71] op_sel_hi:[1,0,1]
	v_pk_fma_f32 v[136:137], v[120:121], s[4:5], v[72:73] op_sel_hi:[1,0,1]
	v_pk_fma_f32 v[138:139], v[122:123], s[4:5], v[74:75] op_sel_hi:[1,0,1]
	v_pk_fma_f32 v[140:141], v[124:125], s[4:5], v[76:77] op_sel_hi:[1,0,1]
	v_pk_fma_f32 v[142:143], v[126:127], s[4:5], v[78:79] op_sel_hi:[1,0,1]
	v_pk_fma_f32 v[144:145], v[128:129], s[4:5], v[80:81] op_sel_hi:[1,0,1]
	v_exp_f32_e32 v130, v130
	v_exp_f32_e32 v131, v131
	v_exp_f32_e32 v132, v132
	v_exp_f32_e32 v133, v133
	v_exp_f32_e32 v134, v134
	v_exp_f32_e32 v135, v135
	v_exp_f32_e32 v136, v136
	v_exp_f32_e32 v137, v137
	v_exp_f32_e32 v138, v138
	v_exp_f32_e32 v139, v139
	v_exp_f32_e32 v140, v140
	v_exp_f32_e32 v141, v141
	v_exp_f32_e32 v142, v142
	v_exp_f32_e32 v143, v143
	v_exp_f32_e32 v144, v144
	v_exp_f32_e32 v145, v145
	v_pk_add_f32 v[130:131], v[130:131], 1.0 op_sel_hi:[1,0]
	v_pk_add_f32 v[132:133], v[132:133], 1.0 op_sel_hi:[1,0]
	v_pk_add_f32 v[134:135], v[134:135], 1.0 op_sel_hi:[1,0]
	v_pk_add_f32 v[136:137], v[136:137], 1.0 op_sel_hi:[1,0]
	v_pk_add_f32 v[138:139], v[138:139], 1.0 op_sel_hi:[1,0]
	v_pk_add_f32 v[140:141], v[140:141], 1.0 op_sel_hi:[1,0]
	v_pk_add_f32 v[142:143], v[142:143], 1.0 op_sel_hi:[1,0]
	v_pk_add_f32 v[144:145], v[144:145], 1.0 op_sel_hi:[1,0]
	v_rcp_f32_e32 v130, v130
	v_rcp_f32_e32 v131, v131
	v_rcp_f32_e32 v132, v132
	v_rcp_f32_e32 v133, v133
	v_rcp_f32_e32 v134, v134
	v_rcp_f32_e32 v135, v135
	v_rcp_f32_e32 v136, v136
	v_rcp_f32_e32 v137, v137
	v_rcp_f32_e32 v138, v138
	v_rcp_f32_e32 v139, v139
	v_rcp_f32_e32 v140, v140
	v_rcp_f32_e32 v141, v141
	v_rcp_f32_e32 v142, v142
	v_rcp_f32_e32 v143, v143
	v_rcp_f32_e32 v144, v144
	v_rcp_f32_e32 v145, v145
	v_pk_fma_f32 v[130:131], v[130:131], 2.0, 1.0 op_sel_hi:[1,0,0] neg_lo:[1,0,0] neg_hi:[1,0,0]
	v_pk_fma_f32 v[132:133], v[132:133], 2.0, 1.0 op_sel_hi:[1,0,0] neg_lo:[1,0,0] neg_hi:[1,0,0]
	v_pk_fma_f32 v[134:135], v[134:135], 2.0, 1.0 op_sel_hi:[1,0,0] neg_lo:[1,0,0] neg_hi:[1,0,0]
	v_pk_fma_f32 v[136:137], v[136:137], 2.0, 1.0 op_sel_hi:[1,0,0] neg_lo:[1,0,0] neg_hi:[1,0,0]
	v_pk_fma_f32 v[138:139], v[138:139], 2.0, 1.0 op_sel_hi:[1,0,0] neg_lo:[1,0,0] neg_hi:[1,0,0]
	v_pk_fma_f32 v[140:141], v[140:141], 2.0, 1.0 op_sel_hi:[1,0,0] neg_lo:[1,0,0] neg_hi:[1,0,0]
	v_pk_fma_f32 v[142:143], v[142:143], 2.0, 1.0 op_sel_hi:[1,0,0] neg_lo:[1,0,0] neg_hi:[1,0,0]
	v_pk_fma_f32 v[144:145], v[144:145], 2.0, 1.0 op_sel_hi:[1,0,0] neg_lo:[1,0,0] neg_hi:[1,0,0]
	v_cvt_pk_f16_f32 v146, v130, v131
	v_cvt_pk_f16_f32 v147, v132, v133
	v_cvt_pk_f16_f32 v148, v134, v135
	v_cvt_pk_f16_f32 v149, v136, v137
	v_cvt_pk_f16_f32 v150, v138, v139
	v_cvt_pk_f16_f32 v151, v140, v141
	v_cvt_pk_f16_f32 v152, v142, v143
	v_cvt_pk_f16_f32 v153, v144, v145
	s_nop 1
	v_permlane32_swap_b32_e32 v146, v148
	v_permlane32_swap_b32_e32 v147, v149
	v_permlane32_swap_b32_e32 v150, v152
	v_permlane32_swap_b32_e32 v151, v153
	global_store_dwordx4 v157, v[146:149], s[32:33] sc1
	global_store_dwordx4 v157, v[150:153], s[32:33] offset:1024 sc1
	s_endpgm
